# final MoE combine: output rows stored with the streaming (nt) hint
# speedup vs baseline: 1.0056x; 1.0056x over previous
; #define GAS __attribute__((address_space(1)))
; __device__ __forceinline__ f32x4 bf4_to_f32(u32x2_g a) { return (f32x4){__uint_as_float(a.x << 16), __uint_as_float(a.x & 0xffff0000u), __uint_as_float(a.y << 16), __uint_as_float(a.y & 0xffff0000u)}; }
; #define lane (lane_id())
; __device__ __forceinline__ void combine_phase(const Ptrs& P, int vcu, int G, int wave, int lane) {
;     ...
; #pragma unroll
;         for (int q = 0; q < 2; ++q) { if (q == 1 && !has1) break;
;             if (pa[q] >= 16384) { const GAS u32x2_t* z0 = (const GAS u32x2_t*)(P.YS + (size_t)MPAD * D + (size_t)pa[q] * D) + lane;
; #pragma unroll
;                 for (int j = 0; j < 8; ++j) ya[q][j] += bf4_to_f32(z0[64 * j]); }
;             if (pb[q] >= 16384) { const GAS u32x2_t* z1 = (const GAS u32x2_t*)(P.YS + (size_t)MPAD * D + (size_t)pb[q] * D) + lane;
; #pragma unroll
;                 for (int j = 0; j < 8; ++j) yb[q][j] += bf4_to_f32(z1[64 * j]); }
;             GAS f32x4* orow = (GAS f32x4*)(P.out + (size_t)mm[q] * D) + lane;
; #pragma unroll
;             for (int j = 0; j < 8; ++j) orow[64 * j] = hv[q][j] + ya[q][j] * ga[q] + yb[q][j] * gb[q]; }
.LBB0_2155:
	v_lshlrev_b32_e32 v96, 16, v16
	v_and_b32_e32 v97, 0xffff0000, v16
	v_lshlrev_b32_e32 v16, 16, v17
	v_and_b32_e32 v17, 0xffff0000, v17
	s_lshl_b64 s[16:17], s[16:17], 13
	v_pk_fma_f32 v[80:81], v[14:15], v[80:81], v[96:97] op_sel_hi:[0,1,1]
	v_pk_fma_f32 v[16:17], v[14:15], v[78:79], v[16:17] op_sel_hi:[0,1,1]
	v_lshlrev_b32_e32 v98, 16, v18
	v_and_b32_e32 v99, 0xffff0000, v18
	v_lshlrev_b32_e32 v100, 16, v19
	v_and_b32_e32 v101, 0xffff0000, v19
	v_lshl_add_u64 v[114:115], v[8:9], 0, s[16:17]
	v_pk_fma_f32 v[18:19], v[14:15], v[94:95], v[16:17] op_sel:[1,0,0]
	v_pk_fma_f32 v[16:17], v[14:15], v[92:93], v[80:81] op_sel:[1,0,0]
	global_store_dwordx4 v[114:115], v[16:19], off nt
	v_lshlrev_b32_e32 v102, 16, v20
	v_and_b32_e32 v103, 0xffff0000, v20
	v_pk_fma_f32 v[16:17], v[14:15], v[76:77], v[98:99] op_sel_hi:[0,1,1]
	v_pk_fma_f32 v[18:19], v[14:15], v[74:75], v[100:101] op_sel_hi:[0,1,1]
	v_lshlrev_b32_e32 v20, 16, v21
	v_and_b32_e32 v21, 0xffff0000, v21
	v_pk_fma_f32 v[18:19], v[14:15], v[90:91], v[18:19] op_sel:[1,0,0]
	v_pk_fma_f32 v[16:17], v[14:15], v[88:89], v[16:17] op_sel:[1,0,0]
	global_store_dwordx4 v[114:115], v[16:19], off offset:1024 nt
	v_lshlrev_b32_e32 v104, 16, v22
	v_and_b32_e32 v105, 0xffff0000, v22
	v_pk_fma_f32 v[16:17], v[14:15], v[72:73], v[102:103] op_sel_hi:[0,1,1]
	v_pk_fma_f32 v[18:19], v[14:15], v[70:71], v[20:21] op_sel_hi:[0,1,1]
	v_lshlrev_b32_e32 v22, 16, v23
	v_and_b32_e32 v23, 0xffff0000, v23
	v_pk_fma_f32 v[18:19], v[14:15], v[86:87], v[18:19] op_sel:[1,0,0]
	v_pk_fma_f32 v[16:17], v[14:15], v[84:85], v[16:17] op_sel:[1,0,0]
	global_store_dwordx4 v[114:115], v[16:19], off offset:2048 nt
	v_lshlrev_b32_e32 v106, 16, v24
	v_and_b32_e32 v107, 0xffff0000, v24
	v_pk_fma_f32 v[16:17], v[14:15], v[68:69], v[104:105] op_sel_hi:[0,1,1]
	v_pk_fma_f32 v[18:19], v[14:15], v[66:67], v[22:23] op_sel_hi:[0,1,1]
	v_lshlrev_b32_e32 v24, 16, v25
	v_and_b32_e32 v25, 0xffff0000, v25
	v_pk_fma_f32 v[18:19], v[14:15], v[82:83], v[18:19] op_sel:[1,0,0]
	v_pk_fma_f32 v[16:17], v[14:15], v[50:51], v[16:17] op_sel:[1,0,0]
	global_store_dwordx4 v[114:115], v[16:19], off offset:3072 nt
	v_add_co_u32_e32 v20, vcc, s38, v114
	s_nop 0
	v_pk_fma_f32 v[16:17], v[14:15], v[64:65], v[106:107] op_sel_hi:[0,1,1]
	v_pk_fma_f32 v[18:19], v[14:15], v[62:63], v[24:25] op_sel_hi:[0,1,1]
	v_lshlrev_b32_e32 v108, 16, v26
	v_and_b32_e32 v109, 0xffff0000, v26
	v_lshlrev_b32_e32 v26, 16, v27
	v_and_b32_e32 v27, 0xffff0000, v27
	v_pk_fma_f32 v[18:19], v[14:15], v[46:47], v[18:19] op_sel:[1,0,0]
	v_pk_fma_f32 v[16:17], v[14:15], v[44:45], v[16:17] op_sel:[1,0,0]
	v_addc_co_u32_e32 v21, vcc, 0, v115, vcc
	global_store_dwordx4 v[20:21], v[16:19], off nt
	v_lshlrev_b32_e32 v110, 16, v28
	v_and_b32_e32 v111, 0xffff0000, v28
	v_pk_fma_f32 v[16:17], v[14:15], v[60:61], v[108:109] op_sel_hi:[0,1,1]
	v_pk_fma_f32 v[18:19], v[14:15], v[58:59], v[26:27] op_sel_hi:[0,1,1]
	v_lshlrev_b32_e32 v28, 16, v29
	v_and_b32_e32 v29, 0xffff0000, v29
	v_pk_fma_f32 v[18:19], v[14:15], v[42:43], v[18:19] op_sel:[1,0,0]
	v_pk_fma_f32 v[16:17], v[14:15], v[40:41], v[16:17] op_sel:[1,0,0]
	global_store_dwordx4 v[20:21], v[16:19], off offset:1024 nt
	v_lshlrev_b32_e32 v112, 16, v30
	v_and_b32_e32 v113, 0xffff0000, v30
	v_pk_fma_f32 v[16:17], v[14:15], v[56:57], v[110:111] op_sel_hi:[0,1,1]
	v_pk_fma_f32 v[18:19], v[14:15], v[54:55], v[28:29] op_sel_hi:[0,1,1]
	v_lshlrev_b32_e32 v30, 16, v31
	v_and_b32_e32 v31, 0xffff0000, v31
	v_pk_fma_f32 v[18:19], v[14:15], v[38:39], v[18:19] op_sel:[1,0,0]
	v_pk_fma_f32 v[16:17], v[14:15], v[36:37], v[16:17] op_sel:[1,0,0]
	global_store_dwordx4 v[20:21], v[16:19], off offset:2048 nt
	s_nop 1
	v_pk_fma_f32 v[18:19], v[14:15], v[52:53], v[112:113] op_sel_hi:[0,1,1]
	v_pk_fma_f32 v[16:17], v[14:15], v[48:49], v[30:31] op_sel_hi:[0,1,1]
	v_pk_fma_f32 v[16:17], v[14:15], v[32:33], v[16:17] op_sel:[1,0,0]
	v_pk_fma_f32 v[14:15], v[14:15], v[34:35], v[18:19] op_sel:[1,0,0]
	global_store_dwordx4 v[20:21], v[14:17], off offset:3072 nt

; #define GAS __attribute__((address_space(1)))
; __device__ __forceinline__ f32x4 bf4_to_f32(u32x2_g a) { return (f32x4){__uint_as_float(a.x << 16), __uint_as_float(a.x & 0xffff0000u), __uint_as_float(a.y << 16), __uint_as_float(a.y & 0xffff0000u)}; }
; #define lane (lane_id())
; __device__ __forceinline__ void combine_phase(const Ptrs& P, int vcu, int G, int wave, int lane) {
;     ...
; #pragma unroll
;         for (int q = 0; q < 2; ++q) { if (q == 1 && !has1) break;
;             if (pa[q] >= 16384) { const GAS u32x2_t* z0 = (const GAS u32x2_t*)(P.YS + (size_t)MPAD * D + (size_t)pa[q] * D) + lane;
; #pragma unroll
;                 for (int j = 0; j < 8; ++j) ya[q][j] += bf4_to_f32(z0[64 * j]); }
;             if (pb[q] >= 16384) { const GAS u32x2_t* z1 = (const GAS u32x2_t*)(P.YS + (size_t)MPAD * D + (size_t)pb[q] * D) + lane;
; #pragma unroll
;                 for (int j = 0; j < 8; ++j) yb[q][j] += bf4_to_f32(z1[64 * j]); }
;             GAS f32x4* orow = (GAS f32x4*)(P.out + (size_t)mm[q] * D) + lane;
; #pragma unroll
;             for (int j = 0; j < 8; ++j) orow[64 * j] = hv[q][j] + ya[q][j] * ga[q] + yb[q][j] * gb[q]; }
.LBB0_2161:
	v_lshlrev_b32_e32 v114, 16, v80
	v_and_b32_e32 v115, 0xffff0000, v80
	v_lshlrev_b32_e32 v80, 16, v81
	v_and_b32_e32 v81, 0xffff0000, v81
	v_lshlrev_b32_e32 v158, 16, v68
	v_and_b32_e32 v159, 0xffff0000, v68
	v_lshlrev_b32_e32 v160, 16, v69
	v_and_b32_e32 v161, 0xffff0000, v69
	v_lshlrev_b32_e32 v162, 16, v66
	v_and_b32_e32 v163, 0xffff0000, v66
	v_lshlrev_b32_e32 v164, 16, v67
	v_and_b32_e32 v165, 0xffff0000, v67
	v_pk_fma_f32 v[66:67], v[48:49], v[112:113], v[114:115] op_sel_hi:[0,1,1]
	v_pk_fma_f32 v[68:69], v[48:49], v[110:111], v[80:81] op_sel_hi:[0,1,1]
	v_lshlrev_b32_e32 v148, 16, v78
	v_and_b32_e32 v149, 0xffff0000, v78
	v_lshlrev_b32_e32 v78, 16, v79
	v_and_b32_e32 v79, 0xffff0000, v79
	v_pk_fma_f32 v[68:69], v[48:49], v[146:147], v[68:69] op_sel:[1,0,0]
	v_pk_fma_f32 v[66:67], v[48:49], v[144:145], v[66:67] op_sel:[1,0,0]
	global_store_dwordx4 v[10:11], v[66:69], off offset:-4096 nt
	v_lshlrev_b32_e32 v150, 16, v76
	v_and_b32_e32 v151, 0xffff0000, v76
	v_pk_fma_f32 v[66:67], v[48:49], v[108:109], v[148:149] op_sel_hi:[0,1,1]
	v_pk_fma_f32 v[68:69], v[48:49], v[106:107], v[78:79] op_sel_hi:[0,1,1]
	v_lshlrev_b32_e32 v76, 16, v77
	v_and_b32_e32 v77, 0xffff0000, v77
	v_pk_fma_f32 v[68:69], v[48:49], v[142:143], v[68:69] op_sel:[1,0,0]
	v_pk_fma_f32 v[66:67], v[48:49], v[140:141], v[66:67] op_sel:[1,0,0]
	global_store_dwordx4 v[10:11], v[66:69], off offset:-3072 nt
	v_lshlrev_b32_e32 v152, 16, v74
	v_and_b32_e32 v153, 0xffff0000, v74
	v_pk_fma_f32 v[66:67], v[48:49], v[104:105], v[150:151] op_sel_hi:[0,1,1]
	v_pk_fma_f32 v[68:69], v[48:49], v[102:103], v[76:77] op_sel_hi:[0,1,1]
	v_lshlrev_b32_e32 v74, 16, v75
	v_and_b32_e32 v75, 0xffff0000, v75
	v_pk_fma_f32 v[68:69], v[48:49], v[138:139], v[68:69] op_sel:[1,0,0]
	v_pk_fma_f32 v[66:67], v[48:49], v[136:137], v[66:67] op_sel:[1,0,0]
	global_store_dwordx4 v[10:11], v[66:69], off offset:-2048 nt
	v_lshlrev_b32_e32 v154, 16, v72
	v_and_b32_e32 v155, 0xffff0000, v72
	v_pk_fma_f32 v[66:67], v[48:49], v[100:101], v[152:153] op_sel_hi:[0,1,1]
	v_pk_fma_f32 v[68:69], v[48:49], v[98:99], v[74:75] op_sel_hi:[0,1,1]
	v_lshlrev_b32_e32 v72, 16, v73
	v_and_b32_e32 v73, 0xffff0000, v73
	v_pk_fma_f32 v[68:69], v[48:49], v[134:135], v[68:69] op_sel:[1,0,0]
	v_pk_fma_f32 v[66:67], v[48:49], v[132:133], v[66:67] op_sel:[1,0,0]
	global_store_dwordx4 v[10:11], v[66:69], off offset:-1024 nt
	v_lshlrev_b32_e32 v156, 16, v70
	v_and_b32_e32 v157, 0xffff0000, v70
	v_pk_fma_f32 v[66:67], v[48:49], v[96:97], v[154:155] op_sel_hi:[0,1,1]
	v_pk_fma_f32 v[68:69], v[48:49], v[94:95], v[72:73] op_sel_hi:[0,1,1]
	v_lshlrev_b32_e32 v70, 16, v71
	v_and_b32_e32 v71, 0xffff0000, v71
	v_pk_fma_f32 v[68:69], v[48:49], v[130:131], v[68:69] op_sel:[1,0,0]
	v_pk_fma_f32 v[66:67], v[48:49], v[128:129], v[66:67] op_sel:[1,0,0]
	global_store_dwordx4 v[10:11], v[66:69], off nt
	s_andn2_b64 vcc, exec, s[22:23]
	s_nop 0
	v_pk_fma_f32 v[66:67], v[48:49], v[92:93], v[156:157] op_sel_hi:[0,1,1]
	v_pk_fma_f32 v[68:69], v[48:49], v[90:91], v[70:71] op_sel_hi:[0,1,1]
	v_pk_fma_f32 v[68:69], v[48:49], v[126:127], v[68:69] op_sel:[1,0,0]
	v_pk_fma_f32 v[66:67], v[48:49], v[124:125], v[66:67] op_sel:[1,0,0]
	global_store_dwordx4 v[10:11], v[66:69], off offset:1024 nt
	s_nop 1
	v_pk_fma_f32 v[66:67], v[48:49], v[88:89], v[158:159] op_sel_hi:[0,1,1]
	v_pk_fma_f32 v[68:69], v[48:49], v[86:87], v[160:161] op_sel_hi:[0,1,1]
	v_pk_fma_f32 v[68:69], v[48:49], v[122:123], v[68:69] op_sel:[1,0,0]
	v_pk_fma_f32 v[66:67], v[48:49], v[120:121], v[66:67] op_sel:[1,0,0]
	global_store_dwordx4 v[10:11], v[66:69], off offset:2048 nt
	s_nop 1
	v_pk_fma_f32 v[66:67], v[48:49], v[84:85], v[162:163] op_sel_hi:[0,1,1]
	v_pk_fma_f32 v[68:69], v[48:49], v[82:83], v[164:165] op_sel_hi:[0,1,1]
	v_pk_fma_f32 v[68:69], v[48:49], v[116:117], v[68:69] op_sel:[1,0,0]
	v_pk_fma_f32 v[66:67], v[48:49], v[118:119], v[66:67] op_sel:[1,0,0]
	global_store_dwordx4 v[10:11], v[66:69], off offset:3072 nt
	s_cbranch_vccnz .LBB0_2156
; #define GAS __attribute__((address_space(1)))
; __device__ __forceinline__ f32x4 bf4_to_f32(u32x2_g a) { return (f32x4){__uint_as_float(a.x << 16), __uint_as_float(a.x & 0xffff0000u), __uint_as_float(a.y << 16), __uint_as_float(a.y & 0xffff0000u)}; }
; #define lane (lane_id())
; __device__ __forceinline__ void combine_phase(const Ptrs& P, int vcu, int G, int wave, int lane) {
;     ...
;         for (int q = 0; q < 2; ++q) { const GAS u32x2_t* y0 = (const GAS u32x2_t*)(P.YS + (size_t)pa[q] * D) + lane; const GAS u32x2_t* y1 = (const GAS u32x2_t*)(P.YS + (size_t)pb[q] * D) + lane;
;             const GAS u32x2_g* hr = (const GAS u32x2_g*)(P.H + (size_t)mm[q] * D) + lane;
; #pragma unroll
;             for (int j = 0; j < 8; ++j) { ya[q][j] = bf4_to_f32(y0[64 * j]); yb[q][j] = bf4_to_f32(y1[64 * j]); hv[q][j] = bf4_to_f32(hr[64 * j]); } }
; #pragma unroll
;         for (int q = 0; q < 2; ++q) { if (q == 1 && !has1) break;
;             if (pa[q] >= 16384) { const GAS u32x2_t* z0 = (const GAS u32x2_t*)(P.YS + (size_t)MPAD * D + (size_t)pa[q] * D) + lane;
; #pragma unroll
;                 for (int j = 0; j < 8; ++j) ya[q][j] += bf4_to_f32(z0[64 * j]); }
;             if (pb[q] >= 16384) { const GAS u32x2_t* z1 = (const GAS u32x2_t*)(P.YS + (size_t)MPAD * D + (size_t)pb[q] * D) + lane;
; #pragma unroll
;                 for (int j = 0; j < 8; ++j) yb[q][j] += bf4_to_f32(z1[64 * j]); }
	s_waitcnt vmcnt(23)
	v_lshlrev_b32_e32 v80, 16, v64
	v_and_b32_e32 v81, 0xffff0000, v64
	v_lshlrev_b32_e32 v78, 16, v65
	v_and_b32_e32 v79, 0xffff0000, v65
	s_waitcnt vmcnt(22)
	v_lshlrev_b32_e32 v76, 16, v62
	v_and_b32_e32 v77, 0xffff0000, v62
	v_lshlrev_b32_e32 v74, 16, v63
	v_and_b32_e32 v75, 0xffff0000, v63
	s_waitcnt vmcnt(21)
	v_lshlrev_b32_e32 v72, 16, v60
	v_and_b32_e32 v73, 0xffff0000, v60
	v_lshlrev_b32_e32 v70, 16, v61
	v_and_b32_e32 v71, 0xffff0000, v61
	s_waitcnt vmcnt(20)
	v_lshlrev_b32_e32 v68, 16, v58
	v_and_b32_e32 v69, 0xffff0000, v58
	v_lshlrev_b32_e32 v66, 16, v59
	v_and_b32_e32 v67, 0xffff0000, v59
	s_waitcnt vmcnt(15)
	v_lshlrev_b32_e32 v64, 16, v56
	v_and_b32_e32 v65, 0xffff0000, v56
	v_lshlrev_b32_e32 v62, 16, v57
	v_and_b32_e32 v63, 0xffff0000, v57
	s_waitcnt vmcnt(14)
	v_lshlrev_b32_e32 v60, 16, v54
	v_and_b32_e32 v61, 0xffff0000, v54
	v_lshlrev_b32_e32 v58, 16, v55
	v_and_b32_e32 v59, 0xffff0000, v55
	s_waitcnt vmcnt(13)
	v_lshlrev_b32_e32 v56, 16, v52
	v_and_b32_e32 v57, 0xffff0000, v52
	v_lshlrev_b32_e32 v54, 16, v53
	v_and_b32_e32 v55, 0xffff0000, v53
	s_waitcnt vmcnt(12)
	v_lshlrev_b32_e32 v52, 16, v50
	v_and_b32_e32 v53, 0xffff0000, v50
	v_lshlrev_b32_e32 v48, 16, v51
	s_cmpk_lt_i32 s24, 0x4000
	v_and_b32_e32 v49, 0xffff0000, v51
	s_cbranch_scc1 .LBB0_2164
	s_mov_b32 s25, s90
	s_lshl_b64 s[22:23], s[24:25], 12
	v_lshl_add_u64 v[50:51], v[6:7], 0, s[22:23]
	global_load_dwordx2 v[166:167], v[50:51], off
	global_load_dwordx2 v[168:169], v[50:51], off offset:512
	global_load_dwordx2 v[170:171], v[50:51], off offset:1024
	global_load_dwordx2 v[172:173], v[50:51], off offset:1536
	global_load_dwordx2 v[174:175], v[50:51], off offset:2048
	global_load_dwordx2 v[176:177], v[50:51], off offset:2560
	global_load_dwordx2 v[178:179], v[50:51], off offset:3072
	global_load_dwordx2 v[180:181], v[50:51], off offset:3584
	s_waitcnt vmcnt(0)
	v_lshlrev_b32_e32 v84, 16, v166
	v_and_b32_e32 v85, 0xffff0000, v166
	v_lshlrev_b32_e32 v82, 16, v167
	v_and_b32_e32 v83, 0xffff0000, v167
	v_pk_add_f32 v[78:79], v[78:79], v[82:83]
	v_pk_add_f32 v[80:81], v[80:81], v[84:85]
	v_lshlrev_b32_e32 v84, 16, v168
	v_and_b32_e32 v85, 0xffff0000, v168
	v_lshlrev_b32_e32 v82, 16, v169
	v_and_b32_e32 v83, 0xffff0000, v169
	v_pk_add_f32 v[74:75], v[74:75], v[82:83]
	v_pk_add_f32 v[76:77], v[76:77], v[84:85]
	v_lshlrev_b32_e32 v84, 16, v170
	v_and_b32_e32 v85, 0xffff0000, v170
	v_lshlrev_b32_e32 v82, 16, v171
	v_and_b32_e32 v83, 0xffff0000, v171
	v_pk_add_f32 v[70:71], v[70:71], v[82:83]
	v_pk_add_f32 v[72:73], v[72:73], v[84:85]
	v_lshlrev_b32_e32 v84, 16, v172
	v_and_b32_e32 v85, 0xffff0000, v172
	v_lshlrev_b32_e32 v82, 16, v173
	v_and_b32_e32 v83, 0xffff0000, v173
	v_pk_add_f32 v[66:67], v[66:67], v[82:83]
	v_pk_add_f32 v[68:69], v[68:69], v[84:85]
	v_lshlrev_b32_e32 v84, 16, v174
	v_and_b32_e32 v85, 0xffff0000, v174
	v_lshlrev_b32_e32 v82, 16, v175
	v_and_b32_e32 v83, 0xffff0000, v175
	v_pk_add_f32 v[62:63], v[62:63], v[82:83]
	v_pk_add_f32 v[64:65], v[64:65], v[84:85]
	v_lshlrev_b32_e32 v84, 16, v176
	v_and_b32_e32 v85, 0xffff0000, v176
	v_lshlrev_b32_e32 v82, 16, v177
	v_and_b32_e32 v83, 0xffff0000, v177
	v_pk_add_f32 v[58:59], v[58:59], v[82:83]
	v_pk_add_f32 v[60:61], v[60:61], v[84:85]
	v_lshlrev_b32_e32 v84, 16, v178
	v_and_b32_e32 v85, 0xffff0000, v178
	v_lshlrev_b32_e32 v82, 16, v179
	v_and_b32_e32 v83, 0xffff0000, v179
	v_pk_add_f32 v[54:55], v[54:55], v[82:83]
	v_lshlrev_b32_e32 v82, 16, v180
	v_and_b32_e32 v83, 0xffff0000, v180
	v_lshlrev_b32_e32 v50, 16, v181
	v_and_b32_e32 v51, 0xffff0000, v181
	v_pk_add_f32 v[56:57], v[56:57], v[84:85]
	v_pk_add_f32 v[48:49], v[48:49], v[50:51]
	v_pk_add_f32 v[52:53], v[52:53], v[82:83]
